# mixer: 2 barriers per chunk, SSD state-update fragment reads hoisted with counted lgkmcnt; conversion ticket atomic decoupled from wave-0 loads; out-proj epilogue residual loads issued 6 steps ahead w
# speedup vs baseline: 1.0045x; 1.0045x over previous
.LBB0_236:
	s_waitcnt lgkmcnt(0)
	s_lshl_b32 s0, s4, 3
	s_add_i32 s0, s0, 0
	s_add_i32 s0, s0, 0x23a00
	v_mov_b32_e32 v97, s0
	ds_read_b32 v96, v97
	v_add_u32_e32 v215, s94, v168
	v_add_u32_e32 v216, s95, v168
	v_add_u32_e32 v217, s86, v168
	v_add_u32_e32 v218, s83, v168
	ds_read_b128 v[68:71], v215
	ds_read_b128 v[72:75], v206
	ds_read_b128 v[76:79], v207 offset:4352
	ds_read_b128 v[80:83], v206 offset:8768
	ds_read_b128 v[84:87], v207 offset:13120
	ds_read_b128 v[220:223], v216
	ds_read_b128 v[224:227], v206 offset:64
	ds_read_b128 v[228:231], v207 offset:4416
	ds_read_b128 v[232:235], v206 offset:8704
	ds_read_b128 v[236:239], v207 offset:13056
	ds_read_b128 v[88:91], v217
	ds_read_b128 v[92:95], v206 offset:128
	ds_read_b128 v[240:243], v207 offset:4480
	ds_read_b128 v[244:247], v206 offset:8896
	s_waitcnt lgkmcnt(14)
	ds_read_b128 v[248:251], v207 offset:13248
	v_pk_mul_f32 v[52:53], v[52:53], v[96:97] op_sel_hi:[1,0]
	v_pk_mul_f32 v[50:51], v[50:51], v[96:97] op_sel_hi:[1,0]
	v_pk_mul_f32 v[56:57], v[56:57], v[96:97] op_sel_hi:[1,0]
	v_pk_mul_f32 v[54:55], v[54:55], v[96:97] op_sel_hi:[1,0]
	v_pk_mul_f32 v[60:61], v[60:61], v[96:97] op_sel_hi:[1,0]
	v_pk_mul_f32 v[58:59], v[58:59], v[96:97] op_sel_hi:[1,0]
	v_pk_mul_f32 v[64:65], v[64:65], v[96:97] op_sel_hi:[1,0]
	v_pk_mul_f32 v[62:63], v[62:63], v[96:97] op_sel_hi:[1,0]
	s_and_b64 s[0:1], s[66:67], s[30:31]
	s_andn2_b64 vcc, exec, s[0:1]
	s_waitcnt lgkmcnt(13)
	v_mfma_f32_16x16x32_bf16 v[50:53], v[68:71], v[72:75], v[50:53]
	s_waitcnt lgkmcnt(12)
	v_mfma_f32_16x16x32_bf16 v[54:57], v[68:71], v[76:79], v[54:57]
	s_waitcnt lgkmcnt(11)
	v_mfma_f32_16x16x32_bf16 v[58:61], v[68:71], v[80:83], v[58:61]
	s_waitcnt lgkmcnt(10)
	v_mfma_f32_16x16x32_bf16 v[62:65], v[68:71], v[84:87], v[62:65]
	ds_read_b128 v[68:71], v218
	ds_read_b128 v[72:75], v206 offset:192
	ds_read_b128 v[76:79], v207 offset:4544
	ds_read_b128 v[80:83], v206 offset:8832
	ds_read_b128 v[84:87], v207 offset:13184
	s_waitcnt lgkmcnt(13)
	v_mfma_f32_16x16x32_bf16 v[50:53], v[220:223], v[224:227], v[50:53]
	s_waitcnt lgkmcnt(12)
	v_mfma_f32_16x16x32_bf16 v[54:57], v[220:223], v[228:231], v[54:57]
	s_waitcnt lgkmcnt(11)
	v_mfma_f32_16x16x32_bf16 v[58:61], v[220:223], v[232:235], v[58:61]
	s_waitcnt lgkmcnt(10)
	v_mfma_f32_16x16x32_bf16 v[62:65], v[220:223], v[236:239], v[62:65]
	s_waitcnt lgkmcnt(8)
	v_mfma_f32_16x16x32_bf16 v[50:53], v[88:91], v[92:95], v[50:53]
	s_waitcnt lgkmcnt(7)
	v_mfma_f32_16x16x32_bf16 v[54:57], v[88:91], v[240:243], v[54:57]
	s_waitcnt lgkmcnt(6)
	v_mfma_f32_16x16x32_bf16 v[58:61], v[88:91], v[244:247], v[58:61]
	s_waitcnt lgkmcnt(5)
	v_mfma_f32_16x16x32_bf16 v[62:65], v[88:91], v[248:251], v[62:65]
	v_cndmask_b32_e64 v96, 0, 1, s[0:1]
	v_cmp_ne_u32_e64 s[30:31], 1, v96
	s_waitcnt lgkmcnt(3)
	v_mfma_f32_16x16x32_bf16 v[50:53], v[68:71], v[72:75], v[50:53]
	s_waitcnt lgkmcnt(2)
	v_mfma_f32_16x16x32_bf16 v[54:57], v[68:71], v[76:79], v[54:57]
	s_waitcnt lgkmcnt(1)
	v_mfma_f32_16x16x32_bf16 v[58:61], v[68:71], v[80:83], v[58:61]
	s_waitcnt lgkmcnt(0)
	v_mfma_f32_16x16x32_bf16 v[62:65], v[68:71], v[84:87], v[62:65]
	s_cbranch_vccnz .LBB0_238
	s_waitcnt vmcnt(12)
	v_pk_add_f32 v[68:69], v[126:127], v[128:129]
	v_mov_b32_e32 v147, 1.0
	v_mul_f32_e32 v70, 0x3fb8aa3b, v68
	v_exp_f32_e32 v70, v70
	s_nop 0
	v_add_f32_e32 v70, 1.0, v70
	v_cmp_gt_f32_e32 vcc, s81, v70
	s_nop 1
	v_cndmask_b32_e64 v71, 0, 32, vcc
	v_ldexp_f32 v70, v70, v71
	v_log_f32_e32 v70, v70
	s_nop 0
	v_mul_f32_e32 v71, 0x3f317217, v70
	v_fma_f32 v71, v70, s44, -v71
	v_fmac_f32_e32 v71, 0x3377d1cf, v70
	v_fmac_f32_e32 v71, 0x3f317217, v70
	v_cmp_lt_f32_e64 s[0:1], |v70|, s84
	s_nop 1
	v_cndmask_b32_e64 v70, v70, v71, s[0:1]
	v_cndmask_b32_e32 v71, 0, v194, vcc
	v_sub_f32_e32 v70, v70, v71
	v_mul_f32_e32 v71, 0x3fb8aa3b, v69
	v_exp_f32_e32 v71, v71
	s_nop 0
	v_add_f32_e32 v71, 1.0, v71
	v_cmp_gt_f32_e32 vcc, s81, v71
	s_nop 1
	v_cndmask_b32_e64 v72, 0, 32, vcc
	v_ldexp_f32 v71, v71, v72
	v_log_f32_e32 v71, v71
	s_nop 0
	v_mul_f32_e32 v72, 0x3f317217, v71
	v_fma_f32 v72, v71, s44, -v72
	v_fmac_f32_e32 v72, 0x3377d1cf, v71
	v_fmac_f32_e32 v72, 0x3f317217, v71
	v_cmp_lt_f32_e64 s[0:1], |v71|, s84
	s_nop 1
	v_cndmask_b32_e64 v71, v71, v72, s[0:1]
	v_cndmask_b32_e32 v72, 0, v194, vcc
	v_cmp_lt_f32_e32 vcc, s45, v68
	v_sub_f32_e32 v71, v71, v72
	v_cmp_lt_f32_e64 s[0:1], s45, v69
	v_cndmask_b32_e32 v138, v70, v68, vcc
	v_add_u32_e32 v70, -1, v99
	v_cndmask_b32_e64 v139, v71, v69, s[0:1]
	v_cmp_lt_i32_e32 vcc, v70, v66
	v_pk_mul_f32 v[68:69], v[138:139], v[136:137]
	s_nop 0
	v_cndmask_b32_e32 v70, v70, v99, vcc
	v_sub_f32_e32 v68, v69, v68
	v_lshlrev_b32_e32 v70, 2, v70
	ds_bpermute_b32 v70, v70, v68
	s_waitcnt lgkmcnt(0)
	v_add_f32_e32 v70, v68, v70
	v_cndmask_b32_e64 v68, v70, v68, s[6:7]
	v_add_u32_e32 v70, -2, v99
	v_cmp_lt_i32_e32 vcc, v70, v66
	s_nop 1
	v_cndmask_b32_e32 v70, v70, v99, vcc
	v_lshlrev_b32_e32 v70, 2, v70
	ds_bpermute_b32 v70, v70, v68
	s_waitcnt lgkmcnt(0)
	v_add_f32_e32 v70, v68, v70
	v_cndmask_b32_e64 v68, v70, v68, s[8:9]
	v_add_u32_e32 v70, -4, v99
	v_cmp_lt_i32_e32 vcc, v70, v66
	s_nop 1
	v_cndmask_b32_e32 v70, v70, v99, vcc
	v_lshlrev_b32_e32 v70, 2, v70
	ds_bpermute_b32 v70, v70, v68
	s_waitcnt lgkmcnt(0)
	v_add_f32_e32 v70, v68, v70
	v_cndmask_b32_e64 v68, v70, v68, s[10:11]
	v_add_u32_e32 v70, -8, v99
	v_cmp_lt_i32_e32 vcc, v70, v66
	s_nop 1
	v_cndmask_b32_e32 v70, v70, v99, vcc
	v_lshlrev_b32_e32 v70, 2, v70
	ds_bpermute_b32 v70, v70, v68
	s_waitcnt lgkmcnt(0)
	v_add_f32_e32 v70, v68, v70
	v_cndmask_b32_e64 v68, v70, v68, s[12:13]
	v_add_u32_e32 v70, -16, v99
	v_cmp_lt_i32_e32 vcc, v70, v66
	s_nop 1
	v_cndmask_b32_e32 v70, v70, v99, vcc
	v_lshlrev_b32_e32 v70, 2, v70
	ds_bpermute_b32 v70, v70, v68
	s_waitcnt lgkmcnt(0)
	v_add_f32_e32 v70, v68, v70
	v_cndmask_b32_e64 v68, v70, v68, s[14:15]
	v_subrev_u32_e32 v70, 32, v99
	v_cmp_lt_i32_e32 vcc, v70, v66
	s_nop 1
	v_cndmask_b32_e32 v70, v70, v99, vcc
	v_lshlrev_b32_e32 v70, 2, v70
	ds_bpermute_b32 v70, v70, v68
	s_waitcnt lgkmcnt(0)
	v_add_f32_e32 v70, v68, v70
	v_cndmask_b32_e64 v70, v70, v68, s[16:17]
	v_sub_f32_e32 v68, v70, v69
	v_lshl_or_b32 v69, v99, 2, v195
	ds_bpermute_b32 v71, v69, v70
	v_mul_f32_e32 v69, 0x3fb8aa3b, v68
	v_exp_f32_e32 v142, v69
	v_mul_f32_e32 v69, 0x3fb8aa3b, v70
	v_xor_b32_e32 v140, 0x80000000, v68
	v_exp_f32_e32 v143, v69
	s_waitcnt lgkmcnt(0)
	v_sub_f32_e32 v68, v71, v68
	v_sub_f32_e32 v69, v71, v70
	v_mul_f32_e32 v68, 0x3fb8aa3b, v68
	v_mul_f32_e32 v69, 0x3fb8aa3b, v69
	v_exp_f32_e32 v68, v68
	v_exp_f32_e32 v69, v69
	v_xor_b32_e32 v141, 0x80000000, v70
	v_pk_mul_f32 v[144:145], v[138:139], v[68:69]
	v_mul_f32_e32 v68, 0x3fb8aa3b, v71
	v_exp_f32_e32 v146, v68

.LBB0_299:
	s_or_b64 exec, exec, s[6:7]
	v_subrev_u32_e32 v101, s3, v1
	s_add_u32 s18, s96, 0x4000000
	s_addc_u32 s19, s97, 0
	s_add_u32 s20, s96, 0x24000000
	s_addc_u32 s21, s97, 0
	s_cmpk_gt_i32 s71, 0x1fff
	s_cbranch_scc0 .LBB0_302
	s_add_i32 s6, s71, 0xffffe000
	s_lshr_b32 s6, s6, 7
	s_mov_b32 s7, 0
	v_readlane_b32 s24, v254, 2
	s_lshl_b64 s[8:9], s[6:7], 22
	s_lshl_b64 s[6:7], s[6:7], 24
	v_readlane_b32 s28, v254, 6
	v_readlane_b32 s29, v254, 7
	s_add_u32 s12, s28, s6
	s_addc_u32 s13, s29, s7
	s_add_u32 s10, s20, s8
	v_readlane_b32 s25, v254, 3
	v_readlane_b32 s26, v254, 4
	v_readlane_b32 s27, v254, 5
	v_readlane_b32 s30, v254, 8
	v_readlane_b32 s31, v254, 9
	s_addc_u32 s11, s21, s9
	s_mov_b32 s9, 4
	s_cbranch_execz .LBB0_303
	s_mov_b64 s[6:7], 0x800
	s_movk_i32 s7, 0x780
	s_branch .LBB0_304

.LBB0_307:
	s_waitcnt vmcnt(0)
	ds_write_b128 v83, v[2:5]
	ds_write_b128 v83, v[6:9] offset:1024
	ds_write_b128 v83, v[10:13] offset:2048
	ds_write_b128 v83, v[14:17] offset:3072
	ds_write_b128 v83, v[18:21] offset:4096
	ds_write_b128 v83, v[22:25] offset:5120
	ds_write_b128 v83, v[26:29] offset:6144
	ds_write_b128 v83, v[30:33] offset:7168
	ds_write_b128 v84, v[34:37] offset:8192
	ds_write_b128 v84, v[38:41] offset:9216
	ds_write_b128 v84, v[42:45] offset:10240
	ds_write_b128 v84, v[46:49] offset:11264
	ds_write_b128 v84, v[50:53] offset:12288
	ds_write_b128 v84, v[54:57] offset:13312
	ds_write_b128 v84, v[58:61] offset:14336
	ds_write_b128 v84, v[62:65] offset:15360
	s_and_saveexec_b64 s[6:7], s[4:5]
	v_add_u32_e32 v1, s3, v101
	v_mov_b32_e32 v85, s22
	ds_write_b32 v85, v1
	s_or_b64 exec, exec, s[6:7]
	v_mov_b32_e32 v85, s22
	s_waitcnt lgkmcnt(0)
	s_barrier
	ds_read_b32 v85, v85
	s_waitcnt lgkmcnt(0)
	v_cmp_lt_i32_e64 s[6:7], s23, v85
	v_readfirstlane_b32 s26, v85
	s_and_b64 vcc, exec, s[6:7]
	s_cbranch_vccnz .LBB0_305
	s_and_saveexec_b64 s[12:13], s[4:5]
	s_cbranch_execz .LBB0_314
	s_mov_b64 s[16:17], exec
	v_mbcnt_lo_u32_b32 v1, s16, 0
	v_mbcnt_hi_u32_b32 v1, s17, v1
	v_cmp_eq_u32_e32 vcc, 0, v1
	s_and_saveexec_b64 s[14:15], vcc
	s_cbranch_execz .LBB0_313
	s_bcnt1_i32_b64 s16, s[16:17]
	v_mov_b32_e32 v2, s16
	global_atomic_add v101, v67, v2, s[0:1] sc0
.LBB0_313:
	s_or_b64 exec, exec, s[14:15]
.LBB0_314:
	s_or_b64 exec, exec, s[12:13]
	s_cmpk_gt_i32 s26, 0x1fff
	s_mov_b64 s[14:15], -1
	s_cbranch_scc0 .LBB0_317
	s_add_i32 s12, s26, 0xffffe000
	s_lshr_b32 s12, s12, 7
	s_mov_b32 s13, s9
	v_readlane_b32 s36, v254, 2
	s_lshl_b64 s[14:15], s[12:13], 22
	s_lshl_b64 s[12:13], s[12:13], 24
	v_readlane_b32 s40, v254, 6
	v_readlane_b32 s41, v254, 7
	s_add_u32 s16, s40, s12
	s_addc_u32 s17, s41, s13
	s_add_u32 s12, s20, s14
	v_readlane_b32 s37, v254, 3
	v_readlane_b32 s38, v254, 4
	v_readlane_b32 s39, v254, 5
	v_readlane_b32 s42, v254, 8
	v_readlane_b32 s43, v254, 9
	s_addc_u32 s13, s21, s15
	s_cbranch_execz .LBB0_318

.LBB0_402:
	v_lshl_add_u32 v154, s8, 8, v160
	v_lshl_or_b32 v10, s42, 8, v161
	v_ashrrev_i32_e32 v155, 31, v154
	v_ashrrev_i32_e32 v11, 31, v10
	v_lshlrev_b64 v[6:7], 11, v[154:155]
	v_lshl_add_u64 v[6:7], v[6:7], 0, v[10:11]
	v_lshl_add_u64 v[184:185], v[6:7], 2, s[64:65]
	v_lshl_add_u64 v[190:191], v[6:7], 1, s[16:17]
	ds_read_b32 v176, v144 offset:44
	ds_read_b32 v178, v144 offset:812
	ds_read_b32 v180, v144 offset:1580
	ds_read_b32 v182, v144 offset:2348
	ds_read_b32 v240, v144 offset:6188
	ds_read_b32 v242, v144 offset:6956
	ds_read_b32 v244, v144 offset:7724
	ds_read_b32 v246, v144 offset:8492
	global_load_dwordx4 v[192:195], v[184:185], off
	global_load_dwordx4 v[196:199], v[184:185], off offset:16
	global_load_dwordx4 v[200:203], v[184:185], off offset:512
	global_load_dwordx4 v[204:207], v[184:185], off offset:528
	s_mov_b64 s[0:1], 0x20000
	v_lshl_add_u64 v[184:185], v[184:185], 0, s[0:1]
	global_load_dwordx4 v[208:211], v[184:185], off
	global_load_dwordx4 v[212:215], v[184:185], off offset:16
	global_load_dwordx4 v[216:219], v[184:185], off offset:512
	global_load_dwordx4 v[220:223], v[184:185], off offset:528
	s_mov_b64 s[0:1], 0x20000
	v_lshl_add_u64 v[184:185], v[184:185], 0, s[0:1]
	global_load_dwordx4 v[224:227], v[184:185], off
	global_load_dwordx4 v[228:231], v[184:185], off offset:16
	global_load_dwordx4 v[232:235], v[184:185], off offset:512
	global_load_dwordx4 v[236:239], v[184:185], off offset:528
	s_waitcnt lgkmcnt(0)
	s_waitcnt vmcnt(10)
	v_pk_fma_f32 v[132:133], v[132:133], v[176:177], v[192:193] op_sel_hi:[1,0,1]
	v_pk_fma_f32 v[134:135], v[134:135], v[176:177], v[194:195] op_sel_hi:[1,0,1]
	v_pk_fma_f32 v[128:129], v[128:129], v[176:177], v[196:197] op_sel_hi:[1,0,1]
	v_pk_fma_f32 v[130:131], v[130:131], v[176:177], v[198:199] op_sel_hi:[1,0,1]
	v_cvt_pk_bf16_f32 v132, v132, v133
	v_cvt_pk_bf16_f32 v133, v134, v135
	v_cvt_pk_bf16_f32 v134, v128, v129
	v_cvt_pk_bf16_f32 v135, v130, v131
	s_nop 1
	global_store_dwordx4 v[190:191], v[132:135], off
	s_mov_b64 s[0:1], 0x20000
	v_lshl_add_u64 v[184:185], v[184:185], 0, s[0:1]
	global_load_dwordx4 v[192:195], v[184:185], off
	global_load_dwordx4 v[196:199], v[184:185], off offset:16
	s_waitcnt vmcnt(11)
	v_pk_fma_f32 v[124:125], v[124:125], v[176:177], v[200:201] op_sel_hi:[1,0,1]
	v_pk_fma_f32 v[126:127], v[126:127], v[176:177], v[202:203] op_sel_hi:[1,0,1]
	v_pk_fma_f32 v[120:121], v[120:121], v[176:177], v[204:205] op_sel_hi:[1,0,1]
	v_pk_fma_f32 v[122:123], v[122:123], v[176:177], v[206:207] op_sel_hi:[1,0,1]
	v_cvt_pk_bf16_f32 v124, v124, v125
	v_cvt_pk_bf16_f32 v125, v126, v127
	v_cvt_pk_bf16_f32 v126, v120, v121
	v_cvt_pk_bf16_f32 v127, v122, v123
	s_nop 1
	global_store_dwordx4 v[190:191], v[124:127], off offset:256
	global_load_dwordx4 v[200:203], v[184:185], off offset:512
	global_load_dwordx4 v[204:207], v[184:185], off offset:528
	s_waitcnt vmcnt(12)
	v_pk_fma_f32 v[116:117], v[116:117], v[178:179], v[208:209] op_sel_hi:[1,0,1]
	v_pk_fma_f32 v[118:119], v[118:119], v[178:179], v[210:211] op_sel_hi:[1,0,1]
	v_pk_fma_f32 v[112:113], v[112:113], v[178:179], v[212:213] op_sel_hi:[1,0,1]
	v_pk_fma_f32 v[114:115], v[114:115], v[178:179], v[214:215] op_sel_hi:[1,0,1]
	v_cvt_pk_bf16_f32 v116, v116, v117
	v_cvt_pk_bf16_f32 v117, v118, v119
	v_cvt_pk_bf16_f32 v118, v112, v113
	v_cvt_pk_bf16_f32 v119, v114, v115
	s_mov_b64 s[0:1], 0x10000
	v_lshl_add_u64 v[190:191], v[190:191], 0, s[0:1]
	global_store_dwordx4 v[190:191], v[116:119], off
	s_mov_b64 s[0:1], 0xa0000
	v_lshl_add_u64 v[184:185], v[184:185], 0, s[0:1]
	global_load_dwordx4 v[208:211], v[184:185], off
	global_load_dwordx4 v[212:215], v[184:185], off offset:16
	s_waitcnt vmcnt(13)
	v_pk_fma_f32 v[108:109], v[108:109], v[178:179], v[216:217] op_sel_hi:[1,0,1]
	v_pk_fma_f32 v[110:111], v[110:111], v[178:179], v[218:219] op_sel_hi:[1,0,1]
	v_pk_fma_f32 v[104:105], v[104:105], v[178:179], v[220:221] op_sel_hi:[1,0,1]
	v_pk_fma_f32 v[106:107], v[106:107], v[178:179], v[222:223] op_sel_hi:[1,0,1]
	v_cvt_pk_bf16_f32 v108, v108, v109
	v_cvt_pk_bf16_f32 v109, v110, v111
	v_cvt_pk_bf16_f32 v110, v104, v105
	v_cvt_pk_bf16_f32 v111, v106, v107
	s_nop 1
	global_store_dwordx4 v[190:191], v[108:111], off offset:256
	global_load_dwordx4 v[216:219], v[184:185], off offset:512
	global_load_dwordx4 v[220:223], v[184:185], off offset:528
	s_waitcnt vmcnt(14)
	v_pk_fma_f32 v[100:101], v[100:101], v[180:181], v[224:225] op_sel_hi:[1,0,1]
	v_pk_fma_f32 v[102:103], v[102:103], v[180:181], v[226:227] op_sel_hi:[1,0,1]
	v_pk_fma_f32 v[96:97], v[96:97], v[180:181], v[228:229] op_sel_hi:[1,0,1]
	v_pk_fma_f32 v[98:99], v[98:99], v[180:181], v[230:231] op_sel_hi:[1,0,1]
	v_cvt_pk_bf16_f32 v100, v100, v101
	v_cvt_pk_bf16_f32 v101, v102, v103
	v_cvt_pk_bf16_f32 v102, v96, v97
	v_cvt_pk_bf16_f32 v103, v98, v99
	s_mov_b64 s[0:1], 0x10000
	v_lshl_add_u64 v[190:191], v[190:191], 0, s[0:1]
	global_store_dwordx4 v[190:191], v[100:103], off
	s_mov_b64 s[0:1], 0x20000
	v_lshl_add_u64 v[184:185], v[184:185], 0, s[0:1]
	global_load_dwordx4 v[224:227], v[184:185], off
	global_load_dwordx4 v[228:231], v[184:185], off offset:16
	s_waitcnt vmcnt(15)
	v_pk_fma_f32 v[92:93], v[92:93], v[180:181], v[232:233] op_sel_hi:[1,0,1]
	v_pk_fma_f32 v[94:95], v[94:95], v[180:181], v[234:235] op_sel_hi:[1,0,1]
	v_pk_fma_f32 v[88:89], v[88:89], v[180:181], v[236:237] op_sel_hi:[1,0,1]
	v_pk_fma_f32 v[90:91], v[90:91], v[180:181], v[238:239] op_sel_hi:[1,0,1]
	v_cvt_pk_bf16_f32 v92, v92, v93
	v_cvt_pk_bf16_f32 v93, v94, v95
	v_cvt_pk_bf16_f32 v94, v88, v89
	v_cvt_pk_bf16_f32 v95, v90, v91
	s_nop 1
	global_store_dwordx4 v[190:191], v[92:95], off offset:256
	global_load_dwordx4 v[232:235], v[184:185], off offset:512
	global_load_dwordx4 v[236:239], v[184:185], off offset:528
	s_waitcnt vmcnt(15)
	v_pk_fma_f32 v[84:85], v[84:85], v[182:183], v[192:193] op_sel_hi:[1,0,1]
	v_pk_fma_f32 v[86:87], v[86:87], v[182:183], v[194:195] op_sel_hi:[1,0,1]
	v_pk_fma_f32 v[80:81], v[80:81], v[182:183], v[196:197] op_sel_hi:[1,0,1]
	v_pk_fma_f32 v[82:83], v[82:83], v[182:183], v[198:199] op_sel_hi:[1,0,1]
	v_cvt_pk_bf16_f32 v84, v84, v85
	v_cvt_pk_bf16_f32 v85, v86, v87
	v_cvt_pk_bf16_f32 v86, v80, v81
	v_cvt_pk_bf16_f32 v87, v82, v83
	s_mov_b64 s[0:1], 0x10000
	v_lshl_add_u64 v[190:191], v[190:191], 0, s[0:1]
	global_store_dwordx4 v[190:191], v[84:87], off
	s_mov_b64 s[0:1], 0x20000
	v_lshl_add_u64 v[184:185], v[184:185], 0, s[0:1]
	global_load_dwordx4 v[192:195], v[184:185], off
	global_load_dwordx4 v[196:199], v[184:185], off offset:16
	s_waitcnt vmcnt(15)
	v_pk_fma_f32 v[76:77], v[76:77], v[182:183], v[200:201] op_sel_hi:[1,0,1]
	v_pk_fma_f32 v[78:79], v[78:79], v[182:183], v[202:203] op_sel_hi:[1,0,1]
	v_pk_fma_f32 v[72:73], v[72:73], v[182:183], v[204:205] op_sel_hi:[1,0,1]
	v_pk_fma_f32 v[74:75], v[74:75], v[182:183], v[206:207] op_sel_hi:[1,0,1]
	v_cvt_pk_bf16_f32 v76, v76, v77
	v_cvt_pk_bf16_f32 v77, v78, v79
	v_cvt_pk_bf16_f32 v78, v72, v73
	v_cvt_pk_bf16_f32 v79, v74, v75
	s_nop 1
	global_store_dwordx4 v[190:191], v[76:79], off offset:256
	global_load_dwordx4 v[200:203], v[184:185], off offset:512
	global_load_dwordx4 v[204:207], v[184:185], off offset:528
	s_waitcnt vmcnt(15)
	v_pk_fma_f32 v[68:69], v[68:69], v[240:241], v[208:209] op_sel_hi:[1,0,1]
	v_pk_fma_f32 v[70:71], v[70:71], v[240:241], v[210:211] op_sel_hi:[1,0,1]
	v_pk_fma_f32 v[64:65], v[64:65], v[240:241], v[212:213] op_sel_hi:[1,0,1]
	v_pk_fma_f32 v[66:67], v[66:67], v[240:241], v[214:215] op_sel_hi:[1,0,1]
	v_cvt_pk_bf16_f32 v68, v68, v69
	v_cvt_pk_bf16_f32 v69, v70, v71
	v_cvt_pk_bf16_f32 v70, v64, v65
	v_cvt_pk_bf16_f32 v71, v66, v67
	s_mov_b64 s[0:1], 0x50000
	v_lshl_add_u64 v[190:191], v[190:191], 0, s[0:1]
	global_store_dwordx4 v[190:191], v[68:71], off
	s_mov_b64 s[0:1], 0x20000
	v_lshl_add_u64 v[184:185], v[184:185], 0, s[0:1]
	global_load_dwordx4 v[208:211], v[184:185], off
	global_load_dwordx4 v[212:215], v[184:185], off offset:16
	s_waitcnt vmcnt(15)
	v_pk_fma_f32 v[60:61], v[60:61], v[240:241], v[216:217] op_sel_hi:[1,0,1]
	v_pk_fma_f32 v[62:63], v[62:63], v[240:241], v[218:219] op_sel_hi:[1,0,1]
	v_pk_fma_f32 v[56:57], v[56:57], v[240:241], v[220:221] op_sel_hi:[1,0,1]
	v_pk_fma_f32 v[58:59], v[58:59], v[240:241], v[222:223] op_sel_hi:[1,0,1]
	v_cvt_pk_bf16_f32 v60, v60, v61
	v_cvt_pk_bf16_f32 v61, v62, v63
	v_cvt_pk_bf16_f32 v62, v56, v57
	v_cvt_pk_bf16_f32 v63, v58, v59
	s_nop 1
	global_store_dwordx4 v[190:191], v[60:63], off offset:256
	global_load_dwordx4 v[216:219], v[184:185], off offset:512
	global_load_dwordx4 v[220:223], v[184:185], off offset:528
	s_waitcnt vmcnt(15)
	v_pk_fma_f32 v[52:53], v[52:53], v[242:243], v[224:225] op_sel_hi:[1,0,1]
	v_pk_fma_f32 v[54:55], v[54:55], v[242:243], v[226:227] op_sel_hi:[1,0,1]
	v_pk_fma_f32 v[48:49], v[48:49], v[242:243], v[228:229] op_sel_hi:[1,0,1]
	v_pk_fma_f32 v[50:51], v[50:51], v[242:243], v[230:231] op_sel_hi:[1,0,1]
	v_cvt_pk_bf16_f32 v52, v52, v53
	v_cvt_pk_bf16_f32 v53, v54, v55
	v_cvt_pk_bf16_f32 v54, v48, v49
	v_cvt_pk_bf16_f32 v55, v50, v51
	s_mov_b64 s[0:1], 0x10000
	v_lshl_add_u64 v[190:191], v[190:191], 0, s[0:1]
	global_store_dwordx4 v[190:191], v[52:55], off
	s_waitcnt vmcnt(13)
	v_pk_fma_f32 v[44:45], v[44:45], v[242:243], v[232:233] op_sel_hi:[1,0,1]
	v_pk_fma_f32 v[46:47], v[46:47], v[242:243], v[234:235] op_sel_hi:[1,0,1]
	v_pk_fma_f32 v[40:41], v[40:41], v[242:243], v[236:237] op_sel_hi:[1,0,1]
	v_pk_fma_f32 v[42:43], v[42:43], v[242:243], v[238:239] op_sel_hi:[1,0,1]
	v_cvt_pk_bf16_f32 v44, v44, v45
	v_cvt_pk_bf16_f32 v45, v46, v47
	v_cvt_pk_bf16_f32 v46, v40, v41
	v_cvt_pk_bf16_f32 v47, v42, v43
	s_nop 1
	global_store_dwordx4 v[190:191], v[44:47], off offset:256
	s_waitcnt vmcnt(11)
	v_pk_fma_f32 v[36:37], v[36:37], v[244:245], v[192:193] op_sel_hi:[1,0,1]
	v_pk_fma_f32 v[38:39], v[38:39], v[244:245], v[194:195] op_sel_hi:[1,0,1]
	v_pk_fma_f32 v[32:33], v[32:33], v[244:245], v[196:197] op_sel_hi:[1,0,1]
	v_pk_fma_f32 v[34:35], v[34:35], v[244:245], v[198:199] op_sel_hi:[1,0,1]
	v_cvt_pk_bf16_f32 v36, v36, v37
	v_cvt_pk_bf16_f32 v37, v38, v39
	v_cvt_pk_bf16_f32 v38, v32, v33
	v_cvt_pk_bf16_f32 v39, v34, v35
	s_mov_b64 s[0:1], 0x10000
	v_lshl_add_u64 v[190:191], v[190:191], 0, s[0:1]
	global_store_dwordx4 v[190:191], v[36:39], off
	s_waitcnt vmcnt(9)
	v_pk_fma_f32 v[28:29], v[28:29], v[244:245], v[200:201] op_sel_hi:[1,0,1]
	v_pk_fma_f32 v[30:31], v[30:31], v[244:245], v[202:203] op_sel_hi:[1,0,1]
	v_pk_fma_f32 v[24:25], v[24:25], v[244:245], v[204:205] op_sel_hi:[1,0,1]
	v_pk_fma_f32 v[26:27], v[26:27], v[244:245], v[206:207] op_sel_hi:[1,0,1]
	v_cvt_pk_bf16_f32 v28, v28, v29
	v_cvt_pk_bf16_f32 v29, v30, v31
	v_cvt_pk_bf16_f32 v30, v24, v25
	v_cvt_pk_bf16_f32 v31, v26, v27
	s_nop 1
	global_store_dwordx4 v[190:191], v[28:31], off offset:256
	s_waitcnt vmcnt(7)
	v_pk_fma_f32 v[20:21], v[20:21], v[246:247], v[208:209] op_sel_hi:[1,0,1]
	v_pk_fma_f32 v[22:23], v[22:23], v[246:247], v[210:211] op_sel_hi:[1,0,1]
	v_pk_fma_f32 v[16:17], v[16:17], v[246:247], v[212:213] op_sel_hi:[1,0,1]
	v_pk_fma_f32 v[18:19], v[18:19], v[246:247], v[214:215] op_sel_hi:[1,0,1]
	v_cvt_pk_bf16_f32 v20, v20, v21
	v_cvt_pk_bf16_f32 v21, v22, v23
	v_cvt_pk_bf16_f32 v22, v16, v17
	v_cvt_pk_bf16_f32 v23, v18, v19
	s_mov_b64 s[0:1], 0x10000
	v_lshl_add_u64 v[190:191], v[190:191], 0, s[0:1]
	global_store_dwordx4 v[190:191], v[20:23], off
	s_waitcnt vmcnt(5)
	v_pk_fma_f32 v[12:13], v[12:13], v[246:247], v[216:217] op_sel_hi:[1,0,1]
	v_pk_fma_f32 v[14:15], v[14:15], v[246:247], v[218:219] op_sel_hi:[1,0,1]
	v_pk_fma_f32 v[2:3], v[2:3], v[246:247], v[220:221] op_sel_hi:[1,0,1]
	v_pk_fma_f32 v[4:5], v[4:5], v[246:247], v[222:223] op_sel_hi:[1,0,1]
	v_cvt_pk_bf16_f32 v12, v12, v13
	v_cvt_pk_bf16_f32 v13, v14, v15
	v_cvt_pk_bf16_f32 v14, v2, v3
	v_cvt_pk_bf16_f32 v15, v4, v5
	s_nop 1
	global_store_dwordx4 v[190:191], v[12:15], off offset:256
	s_mov_b64 s[0:1], -1
	s_andn2_b64 vcc, exec, s[6:7]
	s_cbranch_vccnz .LBB0_388
	s_waitcnt lgkmcnt(0)
	s_barrier
	s_lshl_b64 s[0:1], s[36:37], 8
	v_mov_b32_e32 v11, s1
	v_or_b32_e32 v10, s0, v156
	s_and_saveexec_b64 s[0:1], s[80:81]
	s_xor_b64 s[42:43], exec, s[0:1]
	s_cbranch_execz .LBB0_405
	v_lshlrev_b64 v[2:3], 7, v[10:11]
	v_lshl_add_u64 v[6:7], s[12:13], 0, v[2:3]
	v_lshl_add_u64 v[18:19], v[6:7], 0, s[28:29]
	global_load_dwordx4 v[2:5], v[18:19], off offset:32
	global_load_dwordx4 v[10:13], v[18:19], off offset:16
	v_add_co_u32_e32 v22, vcc, 0x200000, v6
	s_nop 1
	v_addc_co_u32_e32 v23, vcc, 0, v7, vcc
	global_load_dwordx4 v[14:17], v[22:23], off offset:32
	v_lshl_add_u64 v[6:7], v[6:7], 0, s[30:31]
	global_load_dwordx4 v[18:21], v[18:19], off offset:48
	s_nop 0
	global_load_dwordx4 v[22:25], v[22:23], off offset:96
	s_nop 0
	global_load_dwordx4 v[26:29], v[6:7], off offset:16
	s_waitcnt vmcnt(4)
	v_mov_b32_e32 v6, v11
	v_mov_b32_e32 v7, v12
	v_mov_b32_e32 v11, v13
	v_mov_b32_e32 v12, v3
	v_mov_b32_e32 v13, v4
	v_mov_b32_e32 v3, v5
	v_pk_add_f32 v[6:7], v[6:7], v[10:11]
	s_waitcnt vmcnt(3)
	v_mov_b32_e32 v4, v15
	v_mov_b32_e32 v5, v16
	v_mov_b32_e32 v15, v17
	v_pk_add_f32 v[2:3], v[12:13], v[2:3]
	v_add_f32_e32 v1, v6, v7
	v_pk_add_f32 v[4:5], v[4:5], v[14:15]
	v_add_f32_e32 v2, v2, v3
	v_fmamk_f32 v1, v1, 0x3b800000, v174
	v_add_f32_e32 v3, v4, v5
	v_fmamk_f32 v2, v2, 0x3b800000, v174
	v_mul_f32_e32 v4, 0x4f800000, v1
	v_cmp_gt_f32_e32 vcc, s71, v1
	v_fmamk_f32 v3, v3, 0x3b800000, v174
	v_mul_f32_e32 v5, 0x4f800000, v2
	v_cndmask_b32_e32 v1, v1, v4, vcc
	v_cmp_gt_f32_e64 s[0:1], s71, v2
	v_mul_f32_e32 v6, 0x4f800000, v3
	v_sqrt_f32_e32 v4, v1
	v_cndmask_b32_e64 v2, v2, v5, s[0:1]
	v_cmp_gt_f32_e64 s[6:7], s71, v3
	v_sqrt_f32_e32 v5, v2
	v_add_u32_e32 v7, -1, v4
	v_cndmask_b32_e64 v3, v3, v6, s[6:7]
	v_sqrt_f32_e32 v6, v3
	v_add_u32_e32 v10, -1, v5
	v_fma_f32 v14, -v7, v4, v1
	v_add_u32_e32 v9, 1, v4
	v_add_u32_e32 v12, -1, v6
	v_fma_f32 v16, -v10, v5, v2
	v_cmp_ge_f32_e64 s[8:9], 0, v14
	v_add_u32_e32 v11, 1, v5
	v_fma_f32 v15, -v9, v4, v1
	v_fma_f32 v30, -v12, v6, v3
	v_cndmask_b32_e64 v4, v4, v7, s[8:9]
	v_cmp_ge_f32_e64 s[8:9], 0, v16
	v_add_u32_e32 v13, 1, v6
	v_fma_f32 v17, -v11, v5, v2
	v_cndmask_b32_e64 v5, v5, v10, s[8:9]
	v_cmp_ge_f32_e64 s[8:9], 0, v30
	v_fma_f32 v31, -v13, v6, v3
	s_nop 0
	v_cndmask_b32_e64 v6, v6, v12, s[8:9]
	v_cmp_lt_f32_e64 s[8:9], 0, v15
	s_nop 1
	v_cndmask_b32_e64 v4, v4, v9, s[8:9]
	v_cmp_lt_f32_e64 s[8:9], 0, v17
	v_mul_f32_e32 v7, 0x37800000, v4
	v_cndmask_b32_e32 v4, v4, v7, vcc
	v_cndmask_b32_e64 v5, v5, v11, s[8:9]
	v_cmp_lt_f32_e64 s[8:9], 0, v31
	v_mul_f32_e32 v9, 0x37800000, v5
	v_cmp_class_f32_e32 vcc, v1, v175
	v_cndmask_b32_e64 v6, v6, v13, s[8:9]
	v_mul_f32_e32 v10, 0x37800000, v6
	v_cndmask_b32_e64 v5, v5, v9, s[0:1]
	v_cndmask_b32_e32 v1, v4, v1, vcc
	v_cmp_class_f32_e32 vcc, v2, v175
	v_cndmask_b32_e64 v6, v6, v10, s[6:7]
	s_nop 0
	v_cndmask_b32_e32 v7, v5, v2, vcc
	v_cmp_class_f32_e32 vcc, v3, v175
	s_nop 1
	v_cndmask_b32_e32 v2, v6, v3, vcc
	v_div_scale_f32 v3, s[0:1], v1, v1, 1.0
	v_div_scale_f32 v5, s[6:7], v2, v2, 1.0
	v_div_scale_f32 v6, s[6:7], v7, v7, 1.0
	v_rcp_f32_e32 v9, v3
	v_rcp_f32_e32 v11, v5
	v_rcp_f32_e32 v10, v6
	v_div_scale_f32 v4, s[0:1], 1.0, v1, 1.0
	v_fma_f32 v13, -v3, v9, 1.0
	v_fma_f32 v15, -v5, v11, 1.0
	v_div_scale_f32 v12, vcc, 1.0, v2, 1.0
	v_fma_f32 v14, -v6, v10, 1.0
	v_fmac_f32_e32 v9, v13, v9
	v_fmac_f32_e32 v11, v15, v11
	v_fmac_f32_e32 v10, v14, v10
	v_mul_f32_e32 v13, v4, v9
	v_mul_f32_e32 v14, v12, v11
	v_fma_f32 v15, -v3, v13, v4
	v_fma_f32 v16, -v5, v14, v12
	v_fmac_f32_e32 v13, v15, v9
	v_fmac_f32_e32 v14, v16, v11
	v_fma_f32 v3, -v3, v13, v4
	v_fma_f32 v4, -v5, v14, v12
	v_div_fmas_f32 v4, v4, v11, v14
	v_div_fixup_f32 v2, v4, v2, 1.0
	s_waitcnt vmcnt(2)
	v_mov_b32_e32 v4, v19
	v_mov_b32_e32 v5, v20
	v_mov_b32_e32 v19, v21
	v_pk_add_f32 v[4:5], v[4:5], v[18:19]
	s_mov_b64 vcc, s[0:1]
	v_add_f32_e32 v4, v4, v5
	v_fmamk_f32 v4, v4, 0x3b800000, v174
	v_mul_f32_e32 v5, 0x4f800000, v4
	v_cmp_gt_f32_e64 s[0:1], s71, v4
	v_div_fmas_f32 v3, v3, v9, v13
	v_div_fixup_f32 v1, v3, v1, 1.0
	v_cndmask_b32_e64 v4, v4, v5, s[0:1]
	v_div_scale_f32 v3, vcc, 1.0, v7, 1.0
	v_sqrt_f32_e32 v5, v4
	v_mul_f32_e32 v9, v3, v10
	v_fma_f32 v11, -v6, v9, v3
	v_fmac_f32_e32 v9, v11, v10
	v_fma_f32 v3, -v6, v9, v3
	v_add_u32_e32 v6, -1, v5
	v_fma_f32 v11, -v6, v5, v4
	v_cmp_ge_f32_e64 s[6:7], 0, v11
	v_add_u32_e32 v11, 1, v5
	v_div_fmas_f32 v3, v3, v10, v9
	v_cndmask_b32_e64 v6, v5, v6, s[6:7]
	v_fma_f32 v5, -v11, v5, v4
	v_cmp_lt_f32_e64 s[6:7], 0, v5
	s_nop 1
	v_cndmask_b32_e64 v5, v6, v11, s[6:7]
	v_mul_f32_e32 v6, 0x37800000, v5
	v_cndmask_b32_e64 v5, v5, v6, s[0:1]
	v_cmp_class_f32_e64 s[0:1], v4, v175
	s_waitcnt vmcnt(1)
	v_mov_b32_e32 v6, v23
	v_mov_b32_e32 v23, v25
	v_cndmask_b32_e64 v5, v5, v4, s[0:1]
	v_div_fixup_f32 v4, v3, v7, 1.0
	v_mov_b32_e32 v7, v24
	v_div_scale_f32 v11, s[0:1], v5, v5, 1.0
	v_pk_add_f32 v[6:7], v[6:7], v[22:23]
	v_rcp_f32_e32 v12, v11
	v_add_f32_e32 v6, v6, v7
	v_fmamk_f32 v6, v6, 0x3b800000, v174
	v_mul_f32_e32 v7, 0x4f800000, v6
	v_cmp_gt_f32_e64 s[0:1], s71, v6
	v_fma_f32 v3, -v11, v12, 1.0
	v_fmac_f32_e32 v12, v3, v12
	v_cndmask_b32_e64 v6, v6, v7, s[0:1]
	v_sqrt_f32_e32 v7, v6
	v_div_scale_f32 v3, vcc, 1.0, v5, 1.0
	v_mul_f32_e32 v9, v3, v12
	v_fma_f32 v10, -v11, v9, v3
	v_fmac_f32_e32 v9, v10, v12
	v_add_u32_e32 v10, -1, v7
	v_fma_f32 v3, -v11, v9, v3
	v_fma_f32 v11, -v10, v7, v6
	v_cmp_ge_f32_e64 s[6:7], 0, v11
	v_add_u32_e32 v11, 1, v7
	v_div_fmas_f32 v3, v3, v12, v9
	v_cndmask_b32_e64 v10, v7, v10, s[6:7]
	v_fma_f32 v7, -v11, v7, v6
	v_cmp_lt_f32_e64 s[6:7], 0, v7
	v_div_fixup_f32 v3, v3, v5, 1.0
	s_nop 0
	v_cndmask_b32_e64 v7, v10, v11, s[6:7]
	v_mul_f32_e32 v10, 0x37800000, v7
	v_cndmask_b32_e64 v7, v7, v10, s[0:1]
	v_cmp_class_f32_e64 s[0:1], v6, v175
	s_nop 1
	v_cndmask_b32_e64 v10, v7, v6, s[0:1]
	v_div_scale_f32 v11, s[0:1], v10, v10, 1.0
	s_waitcnt vmcnt(0)
	v_mov_b32_e32 v6, v27
	v_mov_b32_e32 v7, v28
	v_mov_b32_e32 v27, v29
	v_rcp_f32_e32 v13, v11
	v_pk_add_f32 v[6:7], v[6:7], v[26:27]
	v_fma_f32 v5, -v11, v13, 1.0
	v_add_f32_e32 v6, v6, v7
	v_fmamk_f32 v6, v6, 0x3b800000, v174
	v_mul_f32_e32 v7, 0x4f800000, v6
	v_cmp_gt_f32_e64 s[0:1], s71, v6
	v_fmac_f32_e32 v13, v5, v13
	v_div_scale_f32 v5, vcc, 1.0, v10, 1.0
	v_cndmask_b32_e64 v6, v6, v7, s[0:1]
	v_sqrt_f32_e32 v7, v6
	v_mul_f32_e32 v9, v5, v13
	v_fma_f32 v12, -v11, v9, v5
	v_fmac_f32_e32 v9, v12, v13
	v_fma_f32 v5, -v11, v9, v5
	v_add_u32_e32 v11, -1, v7
	v_fma_f32 v12, -v11, v7, v6
	v_cmp_ge_f32_e64 s[6:7], 0, v12
	v_add_u32_e32 v12, 1, v7
	v_div_fmas_f32 v5, v5, v13, v9
	v_cndmask_b32_e64 v11, v7, v11, s[6:7]
	v_fma_f32 v7, -v12, v7, v6
	v_cmp_lt_f32_e64 s[6:7], 0, v7
	s_nop 1
	v_cndmask_b32_e64 v7, v11, v12, s[6:7]
	v_mul_f32_e32 v11, 0x37800000, v7
	v_cndmask_b32_e64 v7, v7, v11, s[0:1]
	v_cmp_class_f32_e64 s[0:1], v6, v175
	s_nop 1
	v_cndmask_b32_e64 v7, v7, v6, s[0:1]
	v_div_scale_f32 v11, s[0:1], v7, v7, 1.0
	v_rcp_f32_e32 v12, v11
	v_div_fixup_f32 v6, v5, v10, 1.0
	v_fma_f32 v5, -v11, v12, 1.0
	v_fmac_f32_e32 v12, v5, v12
	v_div_scale_f32 v5, vcc, 1.0, v7, 1.0
	v_mul_f32_e32 v9, v5, v12
	v_fma_f32 v10, -v11, v9, v5
	v_fmac_f32_e32 v9, v10, v12
	v_fma_f32 v5, -v11, v9, v5
	v_div_fmas_f32 v5, v5, v12, v9
	v_div_fixup_f32 v5, v5, v7, 1.0
